# v100 + forget-gate cumsum (NG) done by even-index workgroups (XCD classes with the lighter P1 epilogues) instead of indices 0-7
# baseline (speedup 1.0000x reference)
.LBB0_91:
	v_readlane_b32 s0, v255, 1
	v_readlane_b32 s4, v255, 5
	v_readlane_b32 s1, v255, 2
	v_readlane_b32 s5, v255, 6
	s_cmp_lt_i32 s4, 2
	v_readlane_b32 s2, v255, 3
	v_readlane_b32 s3, v255, 4
	s_cselect_b64 s[0:1], -1, 0
	s_cmp_gt_i32 s5, 1
	s_cselect_b64 s[2:3], -1, 0
	s_and_b64 s[48:49], s[0:1], s[2:3]
	s_andn2_b64 vcc, exec, s[48:49]
	v_readlane_b32 s6, v255, 7
	v_readlane_b32 s7, v255, 8
	s_cbranch_vccnz .LBB0_133
	v_readlane_b32 s0, v255, 0
	s_bfe_u32 s4, s0, 0x10002
	s_and_b32 s1, s0, 3
	s_ashr_i32 s0, s0, 1
	s_and_b32 s0, s0, -4
	s_or_b32 s33, s0, s1
	s_cmp_gt_i32 s33, 15
	s_cbranch_scc1 .LBB0_105
	s_bitcmp1_b32 s33, 0
	s_cbranch_scc1 .LBB0_105
	s_lshl_b32 s0, s4, 3
	s_lshr_b32 s1, s33, 1
	s_add_i32 s0, s0, s1
	s_ashr_i32 s1, s0, 31
	v_readlane_b32 s8, v255, 1
	v_mov_b32_e32 v16, v0
	s_lshl_b64 s[2:3], s[0:1], 14
	v_readlane_b32 s10, v255, 3
	v_readlane_b32 s11, v255, 4
	s_add_u32 s2, s10, s2
	v_lshlrev_b32_e32 v6, 3, v16
	s_addc_u32 s3, s11, s3
	v_ashrrev_i32_e32 v7, 31, v6
	v_lshl_add_u64 v[8:9], v[6:7], 2, s[2:3]
	s_mov_b32 s2, 0x100000
	v_add_co_u32_e32 v2, vcc, s2, v8
	s_mov_b64 s[2:3], 0x100000
	s_nop 0
	v_addc_co_u32_e32 v3, vcc, 0, v9, vcc
	global_load_dwordx4 v[2:5], v[2:3], off
	v_lshl_add_u64 v[8:9], v[8:9], 0, s[2:3]
	global_load_dwordx4 v[12:15], v[8:9], off offset:16
	v_mbcnt_lo_u32_b32 v1, -1, 0
	v_mbcnt_hi_u32_b32 v17, -1, v1
	v_and_b32_e32 v18, 64, v17
	v_add_u32_e32 v8, -1, v17
	v_cmp_lt_i32_e32 vcc, v8, v18
	v_and_b32_e32 v1, 63, v16
	v_readfirstlane_b32 s5, v16
	v_cndmask_b32_e32 v8, v8, v17, vcc
	v_lshlrev_b32_e32 v19, 2, v8
	s_ashr_i32 s6, s5, 6
	v_readlane_b32 s9, v255, 2
	v_readlane_b32 s12, v255, 5
	v_readlane_b32 s13, v255, 6
	v_readlane_b32 s14, v255, 7
	v_readlane_b32 s15, v255, 8
	s_waitcnt vmcnt(1)
	v_add_f32_e32 v3, v2, v3
	v_add_f32_e32 v10, v4, v3
	v_add_f32_e32 v11, v5, v10
	s_waitcnt vmcnt(0)
	v_add_f32_e32 v8, v12, v11
	v_add_f32_e32 v9, v13, v8
	v_add_f32_e32 v4, v14, v9
	v_add_f32_e32 v5, v15, v4
	ds_bpermute_b32 v12, v19, v5
	v_add_u32_e32 v13, -2, v17
	v_cmp_lt_i32_e32 vcc, v13, v18
	v_add_u32_e32 v14, -4, v17
	s_waitcnt lgkmcnt(0)
	v_add_f32_e32 v12, v5, v12
	v_cndmask_b32_e32 v13, v13, v17, vcc
	v_cmp_eq_u32_e32 vcc, 0, v1
	v_lshlrev_b32_e32 v13, 2, v13
	s_nop 0
	v_cndmask_b32_e32 v12, v12, v5, vcc
	ds_bpermute_b32 v13, v13, v12
	v_cmp_lt_i32_e32 vcc, v14, v18
	s_waitcnt lgkmcnt(0)
	v_add_f32_e32 v13, v12, v13
	v_cndmask_b32_e32 v14, v14, v17, vcc
	v_cmp_gt_u32_e32 vcc, 2, v1
	v_lshlrev_b32_e32 v14, 2, v14
	s_nop 0
	v_cndmask_b32_e32 v12, v13, v12, vcc
	ds_bpermute_b32 v13, v14, v12
	v_add_u32_e32 v14, -8, v17
	v_cmp_lt_i32_e32 vcc, v14, v18
	s_waitcnt lgkmcnt(0)
	v_add_f32_e32 v13, v12, v13
	v_cndmask_b32_e32 v14, v14, v17, vcc
	v_cmp_gt_u32_e32 vcc, 4, v1
	v_lshlrev_b32_e32 v14, 2, v14
	s_nop 0
	v_cndmask_b32_e32 v12, v13, v12, vcc
	ds_bpermute_b32 v13, v14, v12
	v_add_u32_e32 v14, -16, v17
	v_cmp_lt_i32_e32 vcc, v14, v18
	s_waitcnt lgkmcnt(0)
	v_add_f32_e32 v13, v12, v13
	v_cndmask_b32_e32 v14, v14, v17, vcc
	v_cmp_gt_u32_e32 vcc, 8, v1
	v_lshlrev_b32_e32 v14, 2, v14
	s_nop 0
	v_cndmask_b32_e32 v12, v13, v12, vcc
	ds_bpermute_b32 v13, v14, v12
	v_subrev_u32_e32 v14, 32, v17
	v_cmp_lt_i32_e32 vcc, v14, v18
	s_waitcnt lgkmcnt(0)
	v_add_f32_e32 v13, v12, v13
	v_cndmask_b32_e32 v14, v14, v17, vcc
	v_cmp_gt_u32_e32 vcc, 16, v1
	v_lshlrev_b32_e32 v14, 2, v14
	s_nop 0
	v_cndmask_b32_e32 v12, v13, v12, vcc
	ds_bpermute_b32 v13, v14, v12
	v_cmp_eq_u32_e32 vcc, 63, v1
	s_waitcnt lgkmcnt(0)
	v_add_f32_e32 v13, v12, v13
	s_and_saveexec_b64 s[2:3], vcc
	s_lshl_b32 s7, s6, 2
	s_add_i32 s7, s7, 0
	v_mov_b32_e32 v14, s7
	ds_write_b32 v14, v13
	s_or_b64 exec, exec, s[2:3]
	s_cmp_lt_i32 s6, 1
	s_waitcnt lgkmcnt(0)
	s_barrier
	s_cbranch_scc1 .LBB0_100
	s_cmp_lt_u32 s6, 8
	s_cbranch_scc1 .LBB0_101
	s_and_b32 s2, s6, 0x7ffffff8
	s_mov_b32 s3, 0
	s_mov_b32 s6, 0
	v_mov_b32_e32 v14, 0
